# split 16 (attention, every 3rd iteration) / 4 (top-k) / 4 (phase 2)
# baseline (speedup 1.0000x reference)
; #define LAS __attribute__((address_space(3)))
; __device__ __forceinline__ void convert_experts(Frame& F, int lo, int hi) {
;     const int gw = F.vcu * 8 + F.wave, NGW = F.G * 8;
;     LAS unsigned char* scr = F.lds + F.wave * 16384;
;     unsigned char* W1t = WSP(F, WS_W1T, unsigned char); unsigned char* W2t = WSP(F, WS_W2T, unsigned char);
;     const float* weg = F.a->in[I_WEG]; const float* weu = F.a->in[I_WEU]; const float* wed = F.a->in[I_WED];
;     const float* wsg = F.a->in[I_WSG]; const float* wsu = F.a->in[I_WSU]; const float* wsd = F.a->in[I_WSD];
;     ...
;     constexpr int NPAIRS = CONV_ITEMS / 2;
;     (void)lo; (void)hi;
;     ...
;     if (gw < NPAIRS) {
;         const int ns = 2 * ((NPAIRS - gw + NGW - 1) / NGW);
;         int sq = 0, r = CONV_RIDX(0);
;         TItem tc, tn; CONV_DESC(r, tc); tn = tc;
;         int p = 0; bool first = true;
.Lcva_vcu:
	s_lshr_b32 s99, s99, 6
	s_lshl_b32 s101, s101, 3
	s_add_u32 s89, s101, s99
	s_movk_i32 s90, 16
	s_lshr_b32 s32, s99, 2
	s_xor_b32 s32, s32, s99
	s_lshr_b32 s100, s89, 3
	s_add_u32 s32, s32, s100
	s_and_b32 s32, s32, 3
	s_cmp_ge_u32 s32, 3
	s_cselect_b32 s99, 3, 0
	s_sub_u32 s32, s32, s99
	s_mov_b32 s95, 0
	s_waitcnt vmcnt(0)
	s_branch .LBB0_304

; #define LAS __attribute__((address_space(3)))
; __device__ __forceinline__ void lds_barrier() { asm volatile("s_waitcnt lgkmcnt(0)\n\ts_barrier" ::: "memory"); }
; __device__ __forceinline__ void phase_attn(Frame& F) {
;     ...
;         lds_barrier();
;         LAS unsigned char* kb = F.lds + buf * ABUF;
;         const bf16x8 q0 = qn0, q1 = qn1;
;         {
;             LAS unsigned char* ob = F.lds + (buf ^ 1) * ABUF;
; #pragma unroll
;             for (int jj = 0; jj < 4; ++jj) { const int ch = tid + 512 * jj, row = ch >> 3, c16 = ch & 7;
;                 *(LAS u32x4*)(ob + row * ATT_ROWB + c16 * 16) = kr[jj]; *(LAS u32x4*)(ob + ATT_VOFF + row * ATT_ROWB + c16 * 16) = vr[jj]; }
;         }
;         const AttnUnit nu = un;
;         un = attn_decode(x8 * PER_X + (jl + 2 * G8 < jlast ? jl + 2 * G8 : jlast)); attn_issue(qkv, un, tid, kr, vr);
;         { const char* qb = (const char*)qkv + (((size_t)nu.b * SEQ + nu.r) * NPROJ + nu.h * 64) * 2; const unsigned qo = __umul24((unsigned)(128 * nu.n + ql), (unsigned)nu.d * (NPROJ * 2)) + 16u * fq;
;           qn0 = *(const bf16x8*)(qb + qo); qn1 = *(const bf16x8*)(qb + qo + 64); }
;         const unsigned qrow = __umul24((unsigned)(128 * cu.n + ql), (unsigned)cu.d);
;         const float c1 = 0.125f * LOG2E;
;         const float nc2 = -__builtin_amdgcn_exp2f(-(float)(cu.h + 1)) * (float)cu.d * LOG2E;
;         const bool first = cu.n == 0;
;         f32x4 St[9];
;         const f32x4 eb = (f32x4){ef[0], ef[1], ef[2], ef[3]} * nc2;
;         float mx = -INFINITY;
;         bf16x8 kf[9][2];
; #pragma unroll
;         for (int T = 0; T < 9; ++T) { LAS unsigned char* ka = kb + (16 * (w + T) + fr) * ATT_ROWB + fq * 16; kf[T][0] = *(LAS bf16x8*)ka; kf[T][1] = *(LAS bf16x8*)(ka + 64); }
.Lcva_wd:
	v_mov_b64_e32 v[48:49], v[4:5]
	v_mov_b64_e32 v[46:47], v[2:3]
	v_mov_b64_e32 v[44:45], v[8:9]
	v_mov_b64_e32 v[42:43], v[6:7]
	s_lshl_b32 s65, 1, s35
	s_waitcnt lgkmcnt(0)
	s_barrier
	s_add_i32 s37, s30, 1
	v_cvt_f32_u32_e32 v54, s37
	v_cvt_f32_u32_e32 v55, s65
	v_add_u32_e32 v110, s85, v82
	v_add_u32_e32 v58, v110, v90
	v_exp_f32_e64 v54, -v54
	v_add_u32_e32 v66, v110, v91
	v_add_u32_e32 v74, v110, v92
	v_add_u32_e32 v111, v110, v93
	v_mul_f32_e32 v79, v55, v54
	ds_read_b128 v[54:57], v58
	ds_read_b128 v[58:61], v58 offset:64
	ds_read_b128 v[62:65], v66
	ds_read_b128 v[66:69], v66 offset:64
	ds_read_b128 v[70:73], v74
	ds_read_b128 v[74:77], v74 offset:64
	ds_read_b128 v[112:115], v111
	ds_read_b128 v[116:119], v111 offset:64
	v_add_u32_e32 v111, v110, v94
	ds_read_b128 v[120:123], v111
	ds_read_b128 v[124:127], v111 offset:64
	v_add_u32_e32 v111, v110, v95
	ds_read_b128 v[128:131], v111
	ds_read_b128 v[132:135], v111 offset:64
	v_add_u32_e32 v111, v110, v96
	ds_read_b128 v[136:139], v111
	ds_read_b128 v[140:143], v111 offset:64
	v_add_u32_e32 v111, v110, v97
	v_add_u32_e32 v110, v110, v98
	ds_read_b128 v[144:147], v111
	ds_read_b128 v[148:151], v111 offset:64
	ds_read_b128 v[152:155], v110
	ds_read_b128 v[156:159], v110 offset:64
	s_sub_u32 s32, s32, 1
	s_cmp_lt_i32 s32, 0
	s_cbranch_scc0 .Lcva_none_l
	s_mov_b32 s32, 2
	s_cmp_eq_u32 s90, 0
	s_cbranch_scc1 .Lcva_none_l
	s_sub_u32 s90, s90, 1
	s_lshr_b32 s98, s89, 6
	s_and_b32 s99, s89, 63
	s_mul_hi_u32 s100, s98, 0xaaaaaaab
	s_lshr_b32 s100, s100, 1
	s_mul_i32 s101, s100, 3
	s_sub_u32 s101, s98, s101
	s_cmp_lt_u32 s100, 256
	s_cselect_b32 s98, 0, 3
	s_cselect_b32 s95, s100, 0
	s_add_u32 s98, s98, s101
	s_lshl_b32 s98, s98, 1
	v_readlane_b32 s96, v253, s98
	s_add_u32 s98, s98, 1
	v_readlane_b32 s97, v253, s98
	s_lshl_b32 s95, s95, 20
	s_nop 3
	s_add_u32 s96, s96, s95
	s_addc_u32 s97, s97, 0
	s_cmp_eq_u32 s101, 2
	s_cbranch_scc1 .Lcva_down_l
	s_lshr_b32 s95, s99, 3
	s_and_b32 s99, s99, 7
	s_lshl_b32 s98, s95, 17
	s_add_u32 s96, s96, s98
	s_addc_u32 s97, s97, 0
	s_lshl_b32 s98, s99, 7
	s_add_u32 s96, s96, s98
	s_addc_u32 s97, s97, 0
	s_lshl_b32 s100, s100, 19
	s_lshr_b32 s98, s99, 2
	s_lshl_b32 s98, s98, 18
	s_add_u32 s100, s100, s98
	s_and_b32 s98, s99, 3
	s_lshl_b32 s98, s98, 15
	s_add_u32 s100, s100, s98
	s_lshl_b32 s98, s101, 17
	s_add_u32 s100, s100, s98
	s_lshl_b32 s98, s95, 7
	s_add_u32 s100, s100, s98
	v_readlane_b32 s92, v253, 12
	v_readlane_b32 s93, v253, 13
	s_mov_b32 s94, 0xc3317218
	s_cmp_eq_u32 s101, 0
	s_cselect_b32 s94, 0xc2b8aa3b, s94
	s_nop 3
	s_add_u32 s92, s92, s100
	s_addc_u32 s93, s93, 0
	s_movk_i32 s95, 0x400
	s_movk_i32 s98, 0x400
	s_branch .Lcva_go_l

; __device__ __forceinline__ void convert_experts(Frame& F, int lo, int hi) {
;     ...
;         for (;;) {
;             const bool more = sq + 1 < ns; const int rn = more ? CONV_RIDX(sq + 1) : r;
;             if (more) { CONV_DESC(rn, tn); titem_issue(tn, F.lane, scr + (p ^ 1) * 8192); }
;             if (!more) asm volatile("s_waitcnt vmcnt(0)" ::: "memory");
;             else if (first) asm volatile("s_waitcnt vmcnt(8)" ::: "memory");
;             else asm volatile("s_waitcnt vmcnt(12)" ::: "memory");
;             titem_finish(tc, F.lane, scr + p * 8192);
;             asm volatile("s_waitcnt lgkmcnt(0)" ::: "memory");
;             if (!more) break;
;             tc = tn; r = rn; ++sq; p ^= 1; first = false;
.Lcva_tail:
	s_cmp_eq_u32 s90, 0
	s_cbranch_scc1 .Lcva_tail_done
	s_mov_b32 s32, 0
	s_mov_b32 s95, 0
	s_sub_u32 s32, s32, 1
	s_cmp_lt_i32 s32, 0
	s_cbranch_scc0 .Lcva_none_t
	s_mov_b32 s32, 2
	s_cmp_eq_u32 s90, 0
	s_cbranch_scc1 .Lcva_none_t
	s_sub_u32 s90, s90, 1
	s_lshr_b32 s98, s89, 6
	s_and_b32 s99, s89, 63
	s_mul_hi_u32 s100, s98, 0xaaaaaaab
	s_lshr_b32 s100, s100, 1
	s_mul_i32 s101, s100, 3
	s_sub_u32 s101, s98, s101
	s_cmp_lt_u32 s100, 256
	s_cselect_b32 s98, 0, 3
	s_cselect_b32 s95, s100, 0
	s_add_u32 s98, s98, s101
	s_lshl_b32 s98, s98, 1
	v_readlane_b32 s96, v253, s98
	s_add_u32 s98, s98, 1
	v_readlane_b32 s97, v253, s98
	s_lshl_b32 s95, s95, 20
	s_nop 3
	s_add_u32 s96, s96, s95
	s_addc_u32 s97, s97, 0
	s_cmp_eq_u32 s101, 2
	s_cbranch_scc1 .Lcva_down_t
	s_lshr_b32 s95, s99, 3
	s_and_b32 s99, s99, 7
	s_lshl_b32 s98, s95, 17
	s_add_u32 s96, s96, s98
	s_addc_u32 s97, s97, 0
	s_lshl_b32 s98, s99, 7
	s_add_u32 s96, s96, s98
	s_addc_u32 s97, s97, 0
	s_lshl_b32 s100, s100, 19
	s_lshr_b32 s98, s99, 2
	s_lshl_b32 s98, s98, 18
	s_add_u32 s100, s100, s98
	s_and_b32 s98, s99, 3
	s_lshl_b32 s98, s98, 15
	s_add_u32 s100, s100, s98
	s_lshl_b32 s98, s101, 17
	s_add_u32 s100, s100, s98
	s_lshl_b32 s98, s95, 7
	s_add_u32 s100, s100, s98
	v_readlane_b32 s92, v253, 12
	v_readlane_b32 s93, v253, 13
	s_mov_b32 s94, 0xc3317218
	s_cmp_eq_u32 s101, 0
	s_cselect_b32 s94, 0xc2b8aa3b, s94
	s_nop 3
	s_add_u32 s92, s92, s100
	s_addc_u32 s93, s93, 0
	s_movk_i32 s95, 0x400
	s_movk_i32 s98, 0x400
	s_branch .Lcva_go_t

; #define LAS __attribute__((address_space(3)))
; __device__ __forceinline__ void router_topk(Frame& F, int tile) {
;     const float* logits = WSP(F, WS_B, float); const float* br = F.a->in[I_BR];
;     int* tk_e = WSP(F, WS_TOPK_E, int); float* tk_g = WSP(F, WS_TOPK_G, float); int* tk_p = WSP(F, WS_TOPK_P, int);
;     int* gcnt = (int*)(F.a->ws + WS_CTL + CTL_CNT);
;     LAS int* hist = (LAS int*)F.lds; LAS int* base = hist + 256;
;     const int lane = F.lane, w = F.wave;
;     if (F.tid < 256) hist[F.tid] = 0;
;     __syncthreads();
;     const f32x4 bias = *(const f32x4*)(br + 4 * lane);
;     f32x4 lgn = *(const f32x4*)(logits + (size_t)(tile * 256 + w * 32) * 256 + 4 * lane);
;     int pe = 0, pp = 0; float pg = 0.f;
;     int* dumpi = (int*)(F.a->ws + WS_B + ((size_t)128 << 20));
.Lcvt_vcu:
	s_add_u32 s69, s41, s40
	s_and_b32 s69, s69, 7
	s_lshl_b32 s41, s41, 3
	s_add_u32 s89, s41, s40
	s_lshl_b32 s71, s64, 3
	s_mul_i32 s39, s71, 16
	s_add_u32 s89, s89, s39
	s_movk_i32 s90, 4
	s_mov_b32 s32, 0
	s_add_u32 s86, s84, 0x9180000
	s_addc_u32 s87, s85, 0
	s_add_u32 s84, s84, 0x1100000
	s_addc_u32 s85, s85, 0
	s_add_u32 s14, s8, 0x900000
	s_addc_u32 s15, s9, 0
	s_add_u32 s16, s8, 0xb00000
	s_addc_u32 s17, s9, 0
	s_add_u32 s18, s8, 0xd00000
	s_addc_u32 s19, s9, 0
	v_mov_b32_e32 v131, 0
	s_add_u32 s20, s8, 0x4000
	v_mov_b32_e32 v133, v131
	s_addc_u32 s21, s9, 0
	v_lshl_add_u64 v[2:3], s[8:9], 0, v[132:133]
	s_mov_b64 s[8:9], 0x1d1c0000
	s_waitcnt vmcnt(0)
	v_lshl_add_u64 v[12:13], v[2:3], 0, s[8:9]
	s_mov_b64 s[8:9], 0x1d1c0100
	s_movk_i32 s4, 0x100
	v_mov_b32_e32 v135, v131
	v_lshl_add_u64 v[14:15], v[2:3], 0, s[8:9]
	s_mov_b64 s[8:9], 0x1d1c0200
	v_cmp_gt_i32_e64 s[4:5], s4, v1
	s_mov_b32 s26, 0
	v_lshl_add_u32 v22, v1, 2, 0
	s_lshl_b32 s27, s49, 5
	v_lshl_add_u64 v[10:11], s[6:7], 0, v[134:135]
	v_cmp_gt_u32_e64 s[6:7], 8, v130
	v_lshl_add_u64 v[16:17], v[2:3], 0, s[8:9]
	v_mov_b64_e32 v[18:19], 0x100
	v_mov_b64_e32 v[20:21], 0xff
	v_mov_b32_e32 v23, 0xff800000
	v_mov_b32_e32 v24, 1
	s_waitcnt vmcnt(0)
	s_barrier
	s_branch .LBB0_532
